# step dispatches to a variant without the second K-half's select ops and MFMAs when the current block ends in the first half of the step
# baseline (speedup 1.0000x reference)
.Lcs_done:
	global_load_dword v241, v4, s[54:55]
	s_add_i32 s18, s13, 32
	s_add_i32 s19, s13, 16
	s_mov_b64 s[6:7], 0
	v_cmp_ge_i32_e32 vcc, s19, v249
	s_and_b64 vcc, exec, vcc
	s_cbranch_vccnz .Lstep_h0
	v_mfma_f32_32x32x16_f16 v[82:97], v[194:197], v[178:181], 0
	v_mfma_f32_32x32x16_f16 v[98:113], v[194:197], v[182:185], 0
	v_add_u32_e32 v14, s13, v243
	v_sub_u32_e32 v3, v230, v14
	v_add_u32_e32 v4, v3, v234
	v_add_u32_e32 v5, -1, v3
	v_med3_i32 v4, v4, -1, 32
	v_med3_i32 v5, v5, -1, 32
	v_cvt_f32_i32_e32 v4, v4
	v_cvt_f32_i32_e32 v5, v5
	v_cvt_pk_f16_f32 v14, v4, v4
	v_cvt_pk_f16_f32 v15, v5, v5
	v_pk_add_f16 v3, v14, s73 neg_lo:[0,1] neg_hi:[0,1]
	v_pk_add_f16 v4, s73, v15 neg_lo:[0,1] neg_hi:[0,1]
	v_pk_min_f16 v6, v3, v4 clamp
	v_pk_add_f16 v5, v14, s74 neg_lo:[0,1] neg_hi:[0,1]
	v_pk_add_f16 v16, s74, v15 neg_lo:[0,1] neg_hi:[0,1]
	v_pk_min_f16 v7, v5, v16 clamp
	v_pk_add_f16 v3, v14, s75 neg_lo:[0,1] neg_hi:[0,1]
	v_pk_add_f16 v4, s75, v15 neg_lo:[0,1] neg_hi:[0,1]
	v_pk_min_f16 v8, v3, v4 clamp
	v_pk_add_f16 v5, v14, s76 neg_lo:[0,1] neg_hi:[0,1]
	v_pk_add_f16 v16, s76, v15 neg_lo:[0,1] neg_hi:[0,1]
	v_pk_min_f16 v9, v5, v16 clamp
	v_pk_add_f16 v3, v14, s77 neg_lo:[0,1] neg_hi:[0,1]
	v_pk_add_f16 v4, s77, v15 neg_lo:[0,1] neg_hi:[0,1]
	v_pk_min_f16 v10, v3, v4 clamp
	v_pk_add_f16 v5, v14, s78 neg_lo:[0,1] neg_hi:[0,1]
	v_pk_add_f16 v16, s78, v15 neg_lo:[0,1] neg_hi:[0,1]
	v_pk_min_f16 v11, v5, v16 clamp
	v_pk_add_f16 v3, v14, s79 neg_lo:[0,1] neg_hi:[0,1]
	v_pk_add_f16 v4, s79, v15 neg_lo:[0,1] neg_hi:[0,1]
	v_pk_min_f16 v12, v3, v4 clamp
	v_pk_add_f16 v5, v14, s80 neg_lo:[0,1] neg_hi:[0,1]
	v_pk_add_f16 v16, s80, v15 neg_lo:[0,1] neg_hi:[0,1]
	v_pk_min_f16 v13, v5, v16 clamp
	v_exp_f32_e32 v82, v82
	v_exp_f32_e32 v83, v83
	v_exp_f32_e32 v84, v84
	v_exp_f32_e32 v85, v85
	v_exp_f32_e32 v86, v86
	v_exp_f32_e32 v87, v87
	v_exp_f32_e32 v88, v88
	v_exp_f32_e32 v89, v89
	v_exp_f32_e32 v90, v90
	v_exp_f32_e32 v91, v91
	v_exp_f32_e32 v92, v92
	v_exp_f32_e32 v93, v93
	v_exp_f32_e32 v94, v94
	v_exp_f32_e32 v95, v95
	v_exp_f32_e32 v96, v96
	v_exp_f32_e32 v97, v97
	v_pk_add_f32 v[82:83], v[82:83], s[82:83]
	v_pk_add_f32 v[84:85], v[84:85], s[82:83]
	v_pk_add_f32 v[86:87], v[86:87], s[82:83]
	v_pk_add_f32 v[88:89], v[88:89], s[82:83]
	v_pk_add_f32 v[90:91], v[90:91], s[82:83]
	v_pk_add_f32 v[92:93], v[92:93], s[82:83]
	v_pk_add_f32 v[94:95], v[94:95], s[82:83]
	v_pk_add_f32 v[96:97], v[96:97], s[82:83]
	v_rcp_f32_e32 v82, v82
	v_rcp_f32_e32 v83, v83
	v_rcp_f32_e32 v84, v84
	v_rcp_f32_e32 v85, v85
	v_rcp_f32_e32 v86, v86
	v_rcp_f32_e32 v87, v87
	v_rcp_f32_e32 v88, v88
	v_rcp_f32_e32 v89, v89
	v_rcp_f32_e32 v90, v90
	v_rcp_f32_e32 v91, v91
	v_rcp_f32_e32 v92, v92
	v_rcp_f32_e32 v93, v93
	v_rcp_f32_e32 v94, v94
	v_rcp_f32_e32 v95, v95
	v_rcp_f32_e32 v96, v96
	v_rcp_f32_e32 v97, v97
	v_cvt_pk_f16_f32 v198, v82, v83
	v_cvt_pk_f16_f32 v199, v84, v85
	v_cvt_pk_f16_f32 v200, v86, v87
	v_cvt_pk_f16_f32 v201, v88, v89
	v_cvt_pk_f16_f32 v202, v90, v91
	v_cvt_pk_f16_f32 v203, v92, v93
	v_cvt_pk_f16_f32 v204, v94, v95
	v_cvt_pk_f16_f32 v205, v96, v97
	v_mfma_f32_32x32x16_f16 v[82:97], v[194:197], v[186:189], 0
	v_exp_f32_e32 v98, v98
	v_exp_f32_e32 v99, v99
	v_exp_f32_e32 v100, v100
	v_exp_f32_e32 v101, v101
	v_exp_f32_e32 v102, v102
	v_exp_f32_e32 v103, v103
	v_mfma_f32_32x32x16_f16 v[66:81], v[198:201], v[6:9], v[66:81]
	v_exp_f32_e32 v104, v104
	v_exp_f32_e32 v105, v105
	v_exp_f32_e32 v106, v106
	v_exp_f32_e32 v107, v107
	v_exp_f32_e32 v108, v108
	v_exp_f32_e32 v109, v109
	v_mfma_f32_32x32x16_f16 v[66:81], v[202:205], v[10:13], v[66:81]
	v_exp_f32_e32 v110, v110
	v_exp_f32_e32 v111, v111
	v_exp_f32_e32 v112, v112
	v_exp_f32_e32 v113, v113
	v_pk_add_f32 v[98:99], v[98:99], s[82:83]
	v_pk_add_f32 v[100:101], v[100:101], s[82:83]
	v_pk_add_f32 v[102:103], v[102:103], s[82:83]
	v_pk_add_f32 v[104:105], v[104:105], s[82:83]
	v_pk_add_f32 v[106:107], v[106:107], s[82:83]
	v_pk_add_f32 v[108:109], v[108:109], s[82:83]
	v_pk_add_f32 v[110:111], v[110:111], s[82:83]
	v_pk_add_f32 v[112:113], v[112:113], s[82:83]
	v_rcp_f32_e32 v98, v98
	v_rcp_f32_e32 v99, v99
	v_rcp_f32_e32 v100, v100
	v_rcp_f32_e32 v101, v101
	v_rcp_f32_e32 v102, v102
	v_rcp_f32_e32 v103, v103
	v_rcp_f32_e32 v104, v104
	v_rcp_f32_e32 v105, v105
	v_rcp_f32_e32 v106, v106
	v_rcp_f32_e32 v107, v107
	v_rcp_f32_e32 v108, v108
	v_rcp_f32_e32 v109, v109
	v_rcp_f32_e32 v110, v110
	v_rcp_f32_e32 v111, v111
	v_rcp_f32_e32 v112, v112
	v_rcp_f32_e32 v113, v113
	v_cvt_pk_f16_f32 v206, v98, v99
	v_cvt_pk_f16_f32 v207, v100, v101
	v_cvt_pk_f16_f32 v208, v102, v103
	v_cvt_pk_f16_f32 v209, v104, v105
	v_cvt_pk_f16_f32 v210, v106, v107
	v_cvt_pk_f16_f32 v211, v108, v109
	v_cvt_pk_f16_f32 v212, v110, v111
	v_cvt_pk_f16_f32 v213, v112, v113
	v_mfma_f32_32x32x16_f16 v[98:113], v[194:197], v[190:193], 0
	v_exp_f32_e32 v82, v82
	v_exp_f32_e32 v83, v83
	v_exp_f32_e32 v84, v84
	v_exp_f32_e32 v85, v85
	v_exp_f32_e32 v86, v86
	v_exp_f32_e32 v87, v87
	v_mfma_f32_32x32x16_f16 v[50:65], v[206:209], v[6:9], v[50:65]
	v_exp_f32_e32 v88, v88
	v_exp_f32_e32 v89, v89
	v_exp_f32_e32 v90, v90
	v_exp_f32_e32 v91, v91
	v_exp_f32_e32 v92, v92
	v_exp_f32_e32 v93, v93
	v_mfma_f32_32x32x16_f16 v[50:65], v[210:213], v[10:13], v[50:65]
	v_exp_f32_e32 v94, v94
	v_exp_f32_e32 v95, v95
	v_exp_f32_e32 v96, v96
	v_exp_f32_e32 v97, v97
	v_pk_add_f32 v[82:83], v[82:83], s[82:83]
	v_pk_add_f32 v[84:85], v[84:85], s[82:83]
	v_pk_add_f32 v[86:87], v[86:87], s[82:83]
	v_pk_add_f32 v[88:89], v[88:89], s[82:83]
	v_pk_add_f32 v[90:91], v[90:91], s[82:83]
	v_pk_add_f32 v[92:93], v[92:93], s[82:83]
	v_pk_add_f32 v[94:95], v[94:95], s[82:83]
	v_pk_add_f32 v[96:97], v[96:97], s[82:83]
	v_rcp_f32_e32 v82, v82
	v_rcp_f32_e32 v83, v83
	v_rcp_f32_e32 v84, v84
	v_rcp_f32_e32 v85, v85
	v_rcp_f32_e32 v86, v86
	v_rcp_f32_e32 v87, v87
	v_rcp_f32_e32 v88, v88
	v_rcp_f32_e32 v89, v89
	v_rcp_f32_e32 v90, v90
	v_rcp_f32_e32 v91, v91
	v_rcp_f32_e32 v92, v92
	v_rcp_f32_e32 v93, v93
	v_rcp_f32_e32 v94, v94
	v_rcp_f32_e32 v95, v95
	v_rcp_f32_e32 v96, v96
	v_rcp_f32_e32 v97, v97
	v_cvt_pk_f16_f32 v214, v82, v83
	v_cvt_pk_f16_f32 v215, v84, v85
	v_cvt_pk_f16_f32 v216, v86, v87
	v_cvt_pk_f16_f32 v217, v88, v89
	v_cvt_pk_f16_f32 v218, v90, v91
	v_cvt_pk_f16_f32 v219, v92, v93
	v_cvt_pk_f16_f32 v220, v94, v95
	v_cvt_pk_f16_f32 v221, v96, v97
	v_exp_f32_e32 v98, v98
	v_exp_f32_e32 v99, v99
	v_exp_f32_e32 v100, v100
	v_exp_f32_e32 v101, v101
	v_exp_f32_e32 v102, v102
	v_exp_f32_e32 v103, v103
	v_mfma_f32_32x32x16_f16 v[34:49], v[214:217], v[6:9], v[34:49]
	v_exp_f32_e32 v104, v104
	v_exp_f32_e32 v105, v105
	v_exp_f32_e32 v106, v106
	v_exp_f32_e32 v107, v107
	v_exp_f32_e32 v108, v108
	v_exp_f32_e32 v109, v109
	v_mfma_f32_32x32x16_f16 v[34:49], v[218:221], v[10:13], v[34:49]
	v_exp_f32_e32 v110, v110
	v_exp_f32_e32 v111, v111
	v_exp_f32_e32 v112, v112
	v_exp_f32_e32 v113, v113
	v_pk_add_f32 v[98:99], v[98:99], s[82:83]
	v_pk_add_f32 v[100:101], v[100:101], s[82:83]
	v_pk_add_f32 v[102:103], v[102:103], s[82:83]
	v_pk_add_f32 v[104:105], v[104:105], s[82:83]
	v_pk_add_f32 v[106:107], v[106:107], s[82:83]
	v_pk_add_f32 v[108:109], v[108:109], s[82:83]
	v_pk_add_f32 v[110:111], v[110:111], s[82:83]
	v_pk_add_f32 v[112:113], v[112:113], s[82:83]
	v_rcp_f32_e32 v98, v98
	v_rcp_f32_e32 v99, v99
	v_rcp_f32_e32 v100, v100
	v_rcp_f32_e32 v101, v101
	v_rcp_f32_e32 v102, v102
	v_rcp_f32_e32 v103, v103
	v_rcp_f32_e32 v104, v104
	v_rcp_f32_e32 v105, v105
	v_rcp_f32_e32 v106, v106
	v_rcp_f32_e32 v107, v107
	v_rcp_f32_e32 v108, v108
	v_rcp_f32_e32 v109, v109
	v_rcp_f32_e32 v110, v110
	v_rcp_f32_e32 v111, v111
	v_rcp_f32_e32 v112, v112
	v_rcp_f32_e32 v113, v113
	v_cvt_pk_f16_f32 v222, v98, v99
	v_cvt_pk_f16_f32 v223, v100, v101
	v_cvt_pk_f16_f32 v224, v102, v103
	v_cvt_pk_f16_f32 v225, v104, v105
	v_cvt_pk_f16_f32 v226, v106, v107
	v_cvt_pk_f16_f32 v227, v108, v109
	v_cvt_pk_f16_f32 v228, v110, v111
	v_cvt_pk_f16_f32 v229, v112, v113
	v_mfma_f32_32x32x16_f16 v[18:33], v[222:225], v[6:9], v[18:33]
	v_add_u32_e32 v194, s13, v243
	v_mfma_f32_32x32x16_f16 v[18:33], v[226:229], v[10:13], v[18:33]
	s_branch .Lpeel_join
.Lstep_h0:
	v_mfma_f32_32x32x16_f16 v[82:97], v[194:197], v[178:181], 0
	v_mfma_f32_32x32x16_f16 v[98:113], v[194:197], v[182:185], 0
	v_add_u32_e32 v14, s13, v243
	v_sub_u32_e32 v3, v230, v14
	v_add_u32_e32 v4, v3, v234
	v_add_u32_e32 v5, -1, v3
	v_med3_i32 v4, v4, -1, 32
	v_med3_i32 v5, v5, -1, 32
	v_cvt_f32_i32_e32 v4, v4
	v_cvt_f32_i32_e32 v5, v5
	v_cvt_pk_f16_f32 v14, v4, v4
	v_cvt_pk_f16_f32 v15, v5, v5
	v_pk_add_f16 v3, v14, s73 neg_lo:[0,1] neg_hi:[0,1]
	v_pk_add_f16 v4, s73, v15 neg_lo:[0,1] neg_hi:[0,1]
	v_pk_min_f16 v6, v3, v4 clamp
	v_pk_add_f16 v5, v14, s74 neg_lo:[0,1] neg_hi:[0,1]
	v_pk_add_f16 v16, s74, v15 neg_lo:[0,1] neg_hi:[0,1]
	v_pk_min_f16 v7, v5, v16 clamp
	v_pk_add_f16 v3, v14, s75 neg_lo:[0,1] neg_hi:[0,1]
	v_pk_add_f16 v4, s75, v15 neg_lo:[0,1] neg_hi:[0,1]
	v_pk_min_f16 v8, v3, v4 clamp
	v_pk_add_f16 v5, v14, s76 neg_lo:[0,1] neg_hi:[0,1]
	v_pk_add_f16 v16, s76, v15 neg_lo:[0,1] neg_hi:[0,1]
	v_pk_min_f16 v9, v5, v16 clamp
	v_exp_f32_e32 v82, v82
	v_exp_f32_e32 v83, v83
	v_exp_f32_e32 v84, v84
	v_exp_f32_e32 v85, v85
	v_exp_f32_e32 v86, v86
	v_exp_f32_e32 v87, v87
	v_exp_f32_e32 v88, v88
	v_exp_f32_e32 v89, v89
	v_exp_f32_e32 v90, v90
	v_exp_f32_e32 v91, v91
	v_exp_f32_e32 v92, v92
	v_exp_f32_e32 v93, v93
	v_exp_f32_e32 v94, v94
	v_exp_f32_e32 v95, v95
	v_exp_f32_e32 v96, v96
	v_exp_f32_e32 v97, v97
	v_pk_add_f32 v[82:83], v[82:83], s[82:83]
	v_pk_add_f32 v[84:85], v[84:85], s[82:83]
	v_pk_add_f32 v[86:87], v[86:87], s[82:83]
	v_pk_add_f32 v[88:89], v[88:89], s[82:83]
	v_pk_add_f32 v[90:91], v[90:91], s[82:83]
	v_pk_add_f32 v[92:93], v[92:93], s[82:83]
	v_pk_add_f32 v[94:95], v[94:95], s[82:83]
	v_pk_add_f32 v[96:97], v[96:97], s[82:83]
	v_rcp_f32_e32 v82, v82
	v_rcp_f32_e32 v83, v83
	v_rcp_f32_e32 v84, v84
	v_rcp_f32_e32 v85, v85
	v_rcp_f32_e32 v86, v86
	v_rcp_f32_e32 v87, v87
	v_rcp_f32_e32 v88, v88
	v_rcp_f32_e32 v89, v89
	v_rcp_f32_e32 v90, v90
	v_rcp_f32_e32 v91, v91
	v_rcp_f32_e32 v92, v92
	v_rcp_f32_e32 v93, v93
	v_rcp_f32_e32 v94, v94
	v_rcp_f32_e32 v95, v95
	v_rcp_f32_e32 v96, v96
	v_rcp_f32_e32 v97, v97
	v_cvt_pk_f16_f32 v198, v82, v83
	v_cvt_pk_f16_f32 v199, v84, v85
	v_cvt_pk_f16_f32 v200, v86, v87
	v_cvt_pk_f16_f32 v201, v88, v89
	v_cvt_pk_f16_f32 v202, v90, v91
	v_cvt_pk_f16_f32 v203, v92, v93
	v_cvt_pk_f16_f32 v204, v94, v95
	v_cvt_pk_f16_f32 v205, v96, v97
	v_mfma_f32_32x32x16_f16 v[82:97], v[194:197], v[186:189], 0
	v_exp_f32_e32 v98, v98
	v_exp_f32_e32 v99, v99
	v_exp_f32_e32 v100, v100
	v_exp_f32_e32 v101, v101
	v_exp_f32_e32 v102, v102
	v_exp_f32_e32 v103, v103
	v_mfma_f32_32x32x16_f16 v[66:81], v[198:201], v[6:9], v[66:81]
	v_exp_f32_e32 v104, v104
	v_exp_f32_e32 v105, v105
	v_exp_f32_e32 v106, v106
	v_exp_f32_e32 v107, v107
	v_exp_f32_e32 v108, v108
	v_exp_f32_e32 v109, v109
	v_exp_f32_e32 v110, v110
	v_exp_f32_e32 v111, v111
	v_exp_f32_e32 v112, v112
	v_exp_f32_e32 v113, v113
	v_pk_add_f32 v[98:99], v[98:99], s[82:83]
	v_pk_add_f32 v[100:101], v[100:101], s[82:83]
	v_pk_add_f32 v[102:103], v[102:103], s[82:83]
	v_pk_add_f32 v[104:105], v[104:105], s[82:83]
	v_pk_add_f32 v[106:107], v[106:107], s[82:83]
	v_pk_add_f32 v[108:109], v[108:109], s[82:83]
	v_pk_add_f32 v[110:111], v[110:111], s[82:83]
	v_pk_add_f32 v[112:113], v[112:113], s[82:83]
	v_rcp_f32_e32 v98, v98
	v_rcp_f32_e32 v99, v99
	v_rcp_f32_e32 v100, v100
	v_rcp_f32_e32 v101, v101
	v_rcp_f32_e32 v102, v102
	v_rcp_f32_e32 v103, v103
	v_rcp_f32_e32 v104, v104
	v_rcp_f32_e32 v105, v105
	v_rcp_f32_e32 v106, v106
	v_rcp_f32_e32 v107, v107
	v_rcp_f32_e32 v108, v108
	v_rcp_f32_e32 v109, v109
	v_rcp_f32_e32 v110, v110
	v_rcp_f32_e32 v111, v111
	v_rcp_f32_e32 v112, v112
	v_rcp_f32_e32 v113, v113
	v_cvt_pk_f16_f32 v206, v98, v99
	v_cvt_pk_f16_f32 v207, v100, v101
	v_cvt_pk_f16_f32 v208, v102, v103
	v_cvt_pk_f16_f32 v209, v104, v105
	v_cvt_pk_f16_f32 v210, v106, v107
	v_cvt_pk_f16_f32 v211, v108, v109
	v_cvt_pk_f16_f32 v212, v110, v111
	v_cvt_pk_f16_f32 v213, v112, v113
	v_mfma_f32_32x32x16_f16 v[98:113], v[194:197], v[190:193], 0
	v_exp_f32_e32 v82, v82
	v_exp_f32_e32 v83, v83
	v_exp_f32_e32 v84, v84
	v_exp_f32_e32 v85, v85
	v_exp_f32_e32 v86, v86
	v_exp_f32_e32 v87, v87
	v_mfma_f32_32x32x16_f16 v[50:65], v[206:209], v[6:9], v[50:65]
	v_exp_f32_e32 v88, v88
	v_exp_f32_e32 v89, v89
	v_exp_f32_e32 v90, v90
	v_exp_f32_e32 v91, v91
	v_exp_f32_e32 v92, v92
	v_exp_f32_e32 v93, v93
	v_exp_f32_e32 v94, v94
	v_exp_f32_e32 v95, v95
	v_exp_f32_e32 v96, v96
	v_exp_f32_e32 v97, v97
	v_pk_add_f32 v[82:83], v[82:83], s[82:83]
	v_pk_add_f32 v[84:85], v[84:85], s[82:83]
	v_pk_add_f32 v[86:87], v[86:87], s[82:83]
	v_pk_add_f32 v[88:89], v[88:89], s[82:83]
	v_pk_add_f32 v[90:91], v[90:91], s[82:83]
	v_pk_add_f32 v[92:93], v[92:93], s[82:83]
	v_pk_add_f32 v[94:95], v[94:95], s[82:83]
	v_pk_add_f32 v[96:97], v[96:97], s[82:83]
	v_rcp_f32_e32 v82, v82
	v_rcp_f32_e32 v83, v83
	v_rcp_f32_e32 v84, v84
	v_rcp_f32_e32 v85, v85
	v_rcp_f32_e32 v86, v86
	v_rcp_f32_e32 v87, v87
	v_rcp_f32_e32 v88, v88
	v_rcp_f32_e32 v89, v89
	v_rcp_f32_e32 v90, v90
	v_rcp_f32_e32 v91, v91
	v_rcp_f32_e32 v92, v92
	v_rcp_f32_e32 v93, v93
	v_rcp_f32_e32 v94, v94
	v_rcp_f32_e32 v95, v95
	v_rcp_f32_e32 v96, v96
	v_rcp_f32_e32 v97, v97
	v_cvt_pk_f16_f32 v214, v82, v83
	v_cvt_pk_f16_f32 v215, v84, v85
	v_cvt_pk_f16_f32 v216, v86, v87
	v_cvt_pk_f16_f32 v217, v88, v89
	v_cvt_pk_f16_f32 v218, v90, v91
	v_cvt_pk_f16_f32 v219, v92, v93
	v_cvt_pk_f16_f32 v220, v94, v95
	v_cvt_pk_f16_f32 v221, v96, v97
	v_exp_f32_e32 v98, v98
	v_exp_f32_e32 v99, v99
	v_exp_f32_e32 v100, v100
	v_exp_f32_e32 v101, v101
	v_exp_f32_e32 v102, v102
	v_exp_f32_e32 v103, v103
	v_mfma_f32_32x32x16_f16 v[34:49], v[214:217], v[6:9], v[34:49]
	v_exp_f32_e32 v104, v104
	v_exp_f32_e32 v105, v105
	v_exp_f32_e32 v106, v106
	v_exp_f32_e32 v107, v107
	v_exp_f32_e32 v108, v108
	v_exp_f32_e32 v109, v109
	v_exp_f32_e32 v110, v110
	v_exp_f32_e32 v111, v111
	v_exp_f32_e32 v112, v112
	v_exp_f32_e32 v113, v113
	v_pk_add_f32 v[98:99], v[98:99], s[82:83]
	v_pk_add_f32 v[100:101], v[100:101], s[82:83]
	v_pk_add_f32 v[102:103], v[102:103], s[82:83]
	v_pk_add_f32 v[104:105], v[104:105], s[82:83]
	v_pk_add_f32 v[106:107], v[106:107], s[82:83]
	v_pk_add_f32 v[108:109], v[108:109], s[82:83]
	v_pk_add_f32 v[110:111], v[110:111], s[82:83]
	v_pk_add_f32 v[112:113], v[112:113], s[82:83]
	v_rcp_f32_e32 v98, v98
	v_rcp_f32_e32 v99, v99
	v_rcp_f32_e32 v100, v100
	v_rcp_f32_e32 v101, v101
	v_rcp_f32_e32 v102, v102
	v_rcp_f32_e32 v103, v103
	v_rcp_f32_e32 v104, v104
	v_rcp_f32_e32 v105, v105
	v_rcp_f32_e32 v106, v106
	v_rcp_f32_e32 v107, v107
	v_rcp_f32_e32 v108, v108
	v_rcp_f32_e32 v109, v109
	v_rcp_f32_e32 v110, v110
	v_rcp_f32_e32 v111, v111
	v_rcp_f32_e32 v112, v112
	v_rcp_f32_e32 v113, v113
	v_cvt_pk_f16_f32 v222, v98, v99
	v_cvt_pk_f16_f32 v223, v100, v101
	v_cvt_pk_f16_f32 v224, v102, v103
	v_cvt_pk_f16_f32 v225, v104, v105
	v_cvt_pk_f16_f32 v226, v106, v107
	v_cvt_pk_f16_f32 v227, v108, v109
	v_cvt_pk_f16_f32 v228, v110, v111
	v_cvt_pk_f16_f32 v229, v112, v113
	v_mfma_f32_32x32x16_f16 v[18:33], v[222:225], v[6:9], v[18:33]
	v_add_u32_e32 v194, s13, v243
	s_branch .Lpeel_join
